# baseline (speedup 1.0000x reference)
_Z6k4_outPKDv8_DF16_S1_PKfS3_S3_Pf:
	s_load_dwordx8 s[4:11], s[0:1], 0x0
	v_lshlrev_b32_e32 v1, 2, v0
	s_load_dwordx4 s[12:15], s[0:1], 0x20
	s_ashr_i32 s0, s2, 7
	v_lshrrev_b32_e32 v48, 4, v0
	s_waitcnt lgkmcnt(0)
	global_load_dword v150, v1, s[8:9]
	global_load_dword v151, v1, s[8:9] offset:1024
	v_mov_b32_e32 v152, v1
	v_lshrrev_b32_e32 v37, 3, v0
	s_ashr_i32 s1, s0, 31
	v_and_b32_e32 v113, 12, v48
	v_and_b32_e32 v49, 4, v37
	s_lshl_b64 s[0:1], s[0:1], 9
	v_lshlrev_b32_e32 v107, 5, v113
	s_lshl_b32 s3, s2, 5
	v_or3_b32 v2, s0, v107, v49
	v_mov_b32_e32 v3, s1
	s_and_b32 s16, s3, 0xfe0
	v_lshlrev_b64 v[2:3], 14, v[2:3]
	s_mov_b32 s9, 0
	v_and_b32_e32 v36, 31, v0
	v_lshl_add_u64 v[2:3], s[12:13], 0, v[2:3]
	s_lshl_b32 s8, s16, 2
	v_mov_b32_e32 v39, 0
	v_lshl_add_u64 v[2:3], v[2:3], 0, s[8:9]
	v_lshlrev_b32_e32 v38, 2, v36
	v_lshl_add_u64 v[12:13], v[2:3], 0, v[38:39]
	s_movk_i32 s17, 0x4000
	v_add_co_u32_e32 v2, vcc, s17, v12
	s_mov_b32 s18, 0x8000
	s_nop 0
	v_addc_co_u32_e32 v3, vcc, 0, v13, vcc
	s_mov_b32 s19, 0xc000
	s_mov_b32 s3, 0x20000
	v_and_b32_e32 v0, 63, v0
	v_lshlrev_b32_e32 v38, 4, v0
	s_add_i32 s8, s2, 0x200
	v_lshl_add_u64 v[40:41], s[4:5], 0, v[38:39]
	v_lshlrev_b32_e32 v44, 10, v113
	v_mov_b32_e32 v45, v39
	s_ashr_i32 s9, s8, 31
	s_lshl_b64 s[8:9], s[8:9], 14
	s_add_i32 s12, s2, 0x400
	s_ashr_i32 s13, s12, 31
	s_lshl_b64 s[12:13], s[12:13], 14
	s_mov_b32 s20, 0x1a8000
	v_or_b32_e32 v42, 0x400, v44
	v_mov_b32_e32 v43, v39
	v_accvgpr_write_b32 a15, 0
	v_accvgpr_write_b32 a14, 0
	v_accvgpr_write_b32 a13, 0
	v_accvgpr_write_b32 a12, 0
	v_accvgpr_write_b32 a11, 0
	v_accvgpr_write_b32 a10, 0
	v_accvgpr_write_b32 a9, 0
	v_accvgpr_write_b32 a8, 0
	v_accvgpr_write_b32 a7, 0
	v_accvgpr_write_b32 a6, 0
	v_accvgpr_write_b32 a5, 0
	v_accvgpr_write_b32 a4, 0
	v_accvgpr_write_b32 a3, 0
	v_accvgpr_write_b32 a2, 0
	v_accvgpr_write_b32 a1, 0
	v_accvgpr_write_b32 a0, 0
	v_accvgpr_write_b32 a31, 0
	v_accvgpr_write_b32 a30, 0
	v_accvgpr_write_b32 a29, 0
	v_accvgpr_write_b32 a28, 0
	v_accvgpr_write_b32 a27, 0
	v_accvgpr_write_b32 a26, 0
	v_accvgpr_write_b32 a25, 0
	v_accvgpr_write_b32 a24, 0
	v_accvgpr_write_b32 a23, 0
	v_accvgpr_write_b32 a22, 0
	v_accvgpr_write_b32 a21, 0
	v_accvgpr_write_b32 a20, 0
	v_accvgpr_write_b32 a19, 0
	v_accvgpr_write_b32 a18, 0
	v_accvgpr_write_b32 a17, 0
	v_accvgpr_write_b32 a16, 0
	v_accvgpr_write_b32 a47, 0
	v_accvgpr_write_b32 a46, 0
	v_accvgpr_write_b32 a45, 0
	v_accvgpr_write_b32 a44, 0
	v_accvgpr_write_b32 a43, 0
	v_accvgpr_write_b32 a42, 0
	v_add_co_u32_e32 v4, vcc, s18, v12
	v_lshl_add_u64 v[0:1], v[40:41], 0, v[44:45]
	s_nop 0
	v_addc_co_u32_e32 v5, vcc, 0, v13, vcc
	v_add_co_u32_e32 v6, vcc, s19, v12
	v_lshl_add_u64 v[24:25], v[0:1], 0, s[12:13]
	s_nop 0
	v_addc_co_u32_e32 v7, vcc, 0, v13, vcc
	v_add_co_u32_e32 v8, vcc, s3, v12
	s_mov_b32 s3, 0x24000
	s_nop 0
	v_addc_co_u32_e32 v9, vcc, 0, v13, vcc
	v_add_co_u32_e32 v10, vcc, s3, v12
	s_mov_b32 s3, 0x28000
	s_nop 0
	v_addc_co_u32_e32 v11, vcc, 0, v13, vcc
	v_add_co_u32_e32 v14, vcc, s3, v12
	s_mov_b32 s3, 0x2c000
	s_nop 0
	v_addc_co_u32_e32 v15, vcc, 0, v13, vcc
	v_add_co_u32_e32 v16, vcc, s3, v12
	s_mov_b32 s3, 0x40000
	s_nop 0
	v_addc_co_u32_e32 v17, vcc, 0, v13, vcc
	global_load_dword v112, v[12:13], off nt
	global_load_dword v111, v[2:3], off nt
	global_load_dword v110, v[4:5], off nt
	global_load_dword v109, v[6:7], off nt
	global_load_dword v108, v[8:9], off nt
	global_load_dword v106, v[10:11], off nt
	global_load_dword v105, v[14:15], off nt
	global_load_dword v104, v[16:17], off nt
	v_add_co_u32_e32 v2, vcc, s3, v12
	s_mov_b32 s3, 0x44000
	s_nop 0
	v_addc_co_u32_e32 v3, vcc, 0, v13, vcc
	v_add_co_u32_e32 v4, vcc, s3, v12
	s_mov_b32 s3, 0x48000
	s_nop 0
	v_addc_co_u32_e32 v5, vcc, 0, v13, vcc
	v_add_co_u32_e32 v6, vcc, s3, v12
	s_mov_b32 s3, 0x4c000
	s_nop 0
	v_addc_co_u32_e32 v7, vcc, 0, v13, vcc
	v_add_co_u32_e32 v8, vcc, s3, v12
	s_mov_b32 s3, 0x60000
	s_nop 0
	v_addc_co_u32_e32 v9, vcc, 0, v13, vcc
	v_add_co_u32_e32 v10, vcc, s3, v12
	s_mov_b32 s3, 0x64000
	s_nop 0
	v_addc_co_u32_e32 v11, vcc, 0, v13, vcc
	v_add_co_u32_e32 v14, vcc, s3, v12
	s_mov_b32 s3, 0x68000
	s_nop 0
	v_addc_co_u32_e32 v15, vcc, 0, v13, vcc
	v_add_co_u32_e32 v16, vcc, s3, v12
	s_mov_b32 s3, 0x6c000
	s_nop 0
	v_addc_co_u32_e32 v17, vcc, 0, v13, vcc
	v_add_co_u32_e32 v18, vcc, s3, v12
	s_mov_b32 s3, 0x80000
	s_nop 0
	v_addc_co_u32_e32 v19, vcc, 0, v13, vcc
	global_load_dword v103, v[2:3], off nt
	global_load_dword v102, v[4:5], off nt
	global_load_dword v101, v[6:7], off nt
	global_load_dword v100, v[8:9], off nt
	global_load_dword v99, v[10:11], off nt
	global_load_dword v98, v[14:15], off nt
	global_load_dword v97, v[16:17], off nt
	global_load_dword v96, v[18:19], off nt
	v_add_co_u32_e32 v2, vcc, s3, v12
	s_mov_b32 s3, 0x84000
	s_nop 0
	v_addc_co_u32_e32 v3, vcc, 0, v13, vcc
	v_add_co_u32_e32 v4, vcc, s3, v12
	s_mov_b32 s3, 0x88000
	s_nop 0
	v_addc_co_u32_e32 v5, vcc, 0, v13, vcc
	v_add_co_u32_e32 v6, vcc, s3, v12
	s_mov_b32 s3, 0x8c000
	s_nop 0
	v_addc_co_u32_e32 v7, vcc, 0, v13, vcc
	v_add_co_u32_e32 v8, vcc, s3, v12
	s_mov_b32 s3, 0xa0000
	s_nop 0
	v_addc_co_u32_e32 v9, vcc, 0, v13, vcc
	v_add_co_u32_e32 v10, vcc, s3, v12
	s_mov_b32 s3, 0xa4000
	s_nop 0
	v_addc_co_u32_e32 v11, vcc, 0, v13, vcc
	v_add_co_u32_e32 v14, vcc, s3, v12
	s_mov_b32 s3, 0xa8000
	s_nop 0
	v_addc_co_u32_e32 v15, vcc, 0, v13, vcc
	v_add_co_u32_e32 v16, vcc, s3, v12
	s_mov_b32 s3, 0xac000
	s_nop 0
	v_addc_co_u32_e32 v17, vcc, 0, v13, vcc
	v_add_co_u32_e32 v18, vcc, s3, v12
	s_mov_b32 s3, 0xc0000
	s_nop 0
	v_addc_co_u32_e32 v19, vcc, 0, v13, vcc
	global_load_dword v95, v[2:3], off nt
	global_load_dword v94, v[4:5], off nt
	global_load_dword v93, v[6:7], off nt
	global_load_dword v92, v[8:9], off nt
	global_load_dword v91, v[10:11], off nt
	global_load_dword v90, v[14:15], off nt
	global_load_dword v89, v[16:17], off nt
	global_load_dword v88, v[18:19], off nt
	v_add_co_u32_e32 v2, vcc, s3, v12
	s_mov_b32 s3, 0xc4000
	s_nop 0
	v_addc_co_u32_e32 v3, vcc, 0, v13, vcc
	v_add_co_u32_e32 v4, vcc, s3, v12
	s_mov_b32 s3, 0xc8000
	s_nop 0
	v_addc_co_u32_e32 v5, vcc, 0, v13, vcc
	v_add_co_u32_e32 v6, vcc, s3, v12
	s_mov_b32 s3, 0xcc000
	s_nop 0
	v_addc_co_u32_e32 v7, vcc, 0, v13, vcc
	v_add_co_u32_e32 v8, vcc, s3, v12
	s_mov_b32 s3, 0xe0000
	s_nop 0
	v_addc_co_u32_e32 v9, vcc, 0, v13, vcc
	v_add_co_u32_e32 v10, vcc, s3, v12
	s_mov_b32 s3, 0xe4000
	s_nop 0
	v_addc_co_u32_e32 v11, vcc, 0, v13, vcc
	v_add_co_u32_e32 v14, vcc, s3, v12
	s_mov_b32 s3, 0xe8000
	s_nop 0
	v_addc_co_u32_e32 v15, vcc, 0, v13, vcc
	v_add_co_u32_e32 v16, vcc, s3, v12
	s_mov_b32 s3, 0xec000
	s_nop 0
	v_addc_co_u32_e32 v17, vcc, 0, v13, vcc
	v_add_co_u32_e32 v18, vcc, s3, v12
	s_mov_b32 s3, 0x100000
	s_nop 0
	v_addc_co_u32_e32 v19, vcc, 0, v13, vcc
	global_load_dword v87, v[2:3], off nt
	global_load_dword v86, v[4:5], off nt
	global_load_dword v85, v[6:7], off nt
	global_load_dword v84, v[8:9], off nt
	global_load_dword v83, v[10:11], off nt
	global_load_dword v82, v[14:15], off nt
	global_load_dword v81, v[16:17], off nt
	global_load_dword v79, v[18:19], off nt
	v_add_co_u32_e32 v2, vcc, s3, v12
	s_mov_b32 s3, 0x104000
	s_nop 0
	v_addc_co_u32_e32 v3, vcc, 0, v13, vcc
	v_add_co_u32_e32 v4, vcc, s3, v12
	s_mov_b32 s3, 0x108000
	s_nop 0
	v_addc_co_u32_e32 v5, vcc, 0, v13, vcc
	v_add_co_u32_e32 v6, vcc, s3, v12
	s_mov_b32 s3, 0x10c000
	s_nop 0
	v_addc_co_u32_e32 v7, vcc, 0, v13, vcc
	v_add_co_u32_e32 v8, vcc, s3, v12
	s_mov_b32 s3, 0x120000
	s_nop 0
	v_addc_co_u32_e32 v9, vcc, 0, v13, vcc
	v_add_co_u32_e32 v10, vcc, s3, v12
	s_mov_b32 s3, 0x124000
	s_nop 0
	v_addc_co_u32_e32 v11, vcc, 0, v13, vcc
	v_add_co_u32_e32 v14, vcc, s3, v12
	s_mov_b32 s3, 0x128000
	s_nop 0
	v_addc_co_u32_e32 v15, vcc, 0, v13, vcc
	v_add_co_u32_e32 v16, vcc, s3, v12
	s_mov_b32 s3, 0x12c000
	s_nop 0
	v_addc_co_u32_e32 v17, vcc, 0, v13, vcc
	v_add_co_u32_e32 v18, vcc, s3, v12
	s_mov_b32 s3, 0x140000
	s_nop 0
	v_addc_co_u32_e32 v19, vcc, 0, v13, vcc
	global_load_dword v71, v[2:3], off nt
	global_load_dword v68, v[4:5], off nt
	global_load_dword v65, v[6:7], off nt
	global_load_dword v63, v[8:9], off nt
	global_load_dword v61, v[10:11], off nt
	global_load_dword v60, v[14:15], off nt
	global_load_dword v59, v[16:17], off nt
	global_load_dword v58, v[18:19], off nt
	v_add_co_u32_e32 v2, vcc, s3, v12
	s_mov_b32 s3, 0x144000
	s_nop 0
	v_addc_co_u32_e32 v3, vcc, 0, v13, vcc
	v_add_co_u32_e32 v4, vcc, s3, v12
	s_mov_b32 s3, 0x148000
	s_nop 0
	v_addc_co_u32_e32 v5, vcc, 0, v13, vcc
	v_add_co_u32_e32 v6, vcc, s3, v12
	s_mov_b32 s3, 0x14c000
	s_nop 0
	v_addc_co_u32_e32 v7, vcc, 0, v13, vcc
	v_add_co_u32_e32 v8, vcc, s3, v12
	s_mov_b32 s3, 0x160000
	s_nop 0
	v_addc_co_u32_e32 v9, vcc, 0, v13, vcc
	v_add_co_u32_e32 v10, vcc, s3, v12
	s_mov_b32 s3, 0x164000
	s_nop 0
	v_addc_co_u32_e32 v11, vcc, 0, v13, vcc
	v_add_co_u32_e32 v14, vcc, s3, v12
	s_mov_b32 s3, 0x168000
	s_nop 0
	v_addc_co_u32_e32 v15, vcc, 0, v13, vcc
	v_add_co_u32_e32 v16, vcc, s3, v12
	s_mov_b32 s3, 0x16c000
	s_nop 0
	v_addc_co_u32_e32 v17, vcc, 0, v13, vcc
	v_add_co_u32_e32 v18, vcc, s3, v12
	s_mov_b32 s3, 0x180000
	s_nop 0
	v_addc_co_u32_e32 v19, vcc, 0, v13, vcc
	global_load_dword v57, v[2:3], off nt
	global_load_dword v56, v[4:5], off nt
	global_load_dword v55, v[6:7], off nt
	global_load_dword v54, v[8:9], off nt
	global_load_dword v53, v[10:11], off nt
	global_load_dword v52, v[14:15], off nt
	global_load_dword v51, v[16:17], off nt
	global_load_dword v50, v[18:19], off nt
	v_add_co_u32_e32 v2, vcc, s3, v12
	s_mov_b32 s3, 0x184000
	s_nop 0
	v_addc_co_u32_e32 v3, vcc, 0, v13, vcc
	v_add_co_u32_e32 v4, vcc, s3, v12
	s_mov_b32 s3, 0x188000
	s_nop 0
	v_addc_co_u32_e32 v5, vcc, 0, v13, vcc
	v_add_co_u32_e32 v6, vcc, s3, v12
	s_mov_b32 s3, 0x18c000
	s_nop 0
	v_addc_co_u32_e32 v7, vcc, 0, v13, vcc
	v_add_co_u32_e32 v8, vcc, s3, v12
	s_mov_b32 s3, 0x1a0000
	s_nop 0
	v_addc_co_u32_e32 v9, vcc, 0, v13, vcc
	v_add_co_u32_e32 v10, vcc, s3, v12
	s_mov_b32 s3, 0x1a4000
	s_nop 0
	v_addc_co_u32_e32 v11, vcc, 0, v13, vcc
	v_add_co_u32_e32 v14, vcc, s3, v12
	s_ashr_i32 s3, s2, 31
	s_lshl_b64 s[4:5], s[2:3], 14
	v_lshl_add_u64 v[16:17], v[0:1], 0, s[4:5]
	v_lshl_add_u64 v[18:19], v[0:1], 0, s[8:9]
	s_addk_i32 s2, 0x600
	global_load_dwordx4 v[20:23], v[16:17], off
	s_nop 0
	global_load_dwordx4 v[16:19], v[18:19], off
	s_ashr_i32 s3, s2, 31
	s_lshl_b64 s[2:3], s[2:3], 14
	v_lshl_add_u64 v[0:1], v[0:1], 0, s[2:3]
	global_load_dwordx4 v[24:27], v[24:25], off
	s_nop 0
	global_load_dwordx4 v[28:31], v[0:1], off
	v_addc_co_u32_e32 v15, vcc, 0, v13, vcc
	v_add_co_u32_e32 v0, vcc, s20, v12
	s_mov_b32 s20, 0x1ac000
	s_nop 0
	v_addc_co_u32_e32 v1, vcc, 0, v13, vcc
	v_add_co_u32_e32 v32, vcc, s20, v12
	s_mov_b32 s20, 0x1c0000
	s_nop 0
	v_addc_co_u32_e32 v33, vcc, 0, v13, vcc
	global_load_dword v80, v[2:3], off nt
	global_load_dword v78, v[4:5], off nt
	global_load_dword v77, v[6:7], off nt
	global_load_dword v76, v[8:9], off nt
	global_load_dword v75, v[10:11], off nt
	global_load_dword v74, v[14:15], off nt
	global_load_dword v72, v[0:1], off nt
	global_load_dword v69, v[32:33], off nt
	v_add_co_u32_e32 v32, vcc, s20, v12
	s_mov_b32 s20, 0x1c4000
	s_nop 0
	v_addc_co_u32_e32 v33, vcc, 0, v13, vcc
	v_add_co_u32_e32 v34, vcc, s20, v12
	s_mov_b32 s20, 0x1c8000
	s_nop 0
	v_addc_co_u32_e32 v35, vcc, 0, v13, vcc
	v_lshl_add_u64 v[14:15], v[40:41], 0, v[42:43]
	v_add_co_u32_e32 v46, vcc, s20, v12
	v_lshl_add_u64 v[0:1], v[14:15], 0, s[4:5]
	v_lshl_add_u64 v[2:3], v[14:15], 0, s[8:9]
	v_addc_co_u32_e32 v47, vcc, 0, v13, vcc
	s_mov_b32 s20, 0x1cc000
	global_load_dwordx4 v[8:11], v[0:1], off
	s_nop 0
	global_load_dwordx4 v[0:3], v[2:3], off
	v_add_co_u32_e32 v114, vcc, s20, v12
	v_lshl_add_u64 v[4:5], v[14:15], 0, s[12:13]
	s_nop 0
	v_addc_co_u32_e32 v115, vcc, 0, v13, vcc
	s_mov_b32 s20, 0x1e0000
	global_load_dwordx4 v[4:7], v[4:5], off
	v_add_co_u32_e32 v116, vcc, s20, v12
	s_mov_b32 s20, 0x1e4000
	s_nop 0
	v_addc_co_u32_e32 v117, vcc, 0, v13, vcc
	v_add_co_u32_e32 v118, vcc, s20, v12
	s_mov_b32 s20, 0x1e8000
	s_nop 0
	v_addc_co_u32_e32 v119, vcc, 0, v13, vcc
	v_add_co_u32_e32 v120, vcc, s20, v12
	s_mov_b32 s20, 0x1ec000
	s_nop 0
	v_addc_co_u32_e32 v121, vcc, 0, v13, vcc
	v_add_co_u32_e32 v122, vcc, s20, v12
	v_accvgpr_write_b32 a41, 0
	s_nop 0
	v_addc_co_u32_e32 v123, vcc, 0, v13, vcc
	v_lshl_add_u64 v[12:13], v[14:15], 0, s[2:3]
	global_load_dwordx4 v[12:15], v[12:13], off
	s_nop 0
	global_load_dword v73, v[32:33], off nt
	global_load_dword v70, v[34:35], off nt
	global_load_dword v67, v[46:47], off nt
	global_load_dword v66, v[114:115], off nt
	global_load_dword v64, v[116:117], off nt
	global_load_dword v62, v[118:119], off nt
	global_load_dword v45, v[120:121], off nt
	global_load_dword v43, v[122:123], off nt
	v_accvgpr_write_b32 a40, 0
	v_accvgpr_write_b32 a39, 0
	v_accvgpr_write_b32 a38, 0
	v_accvgpr_write_b32 a37, 0
	v_accvgpr_write_b32 a36, 0
	v_accvgpr_write_b32 a35, 0
	v_accvgpr_write_b32 a34, 0
	v_accvgpr_write_b32 a33, 0
	v_accvgpr_write_b32 a32, 0
	v_accvgpr_write_b32 a63, 0
	v_accvgpr_write_b32 a62, 0
	v_accvgpr_write_b32 a61, 0
	v_accvgpr_write_b32 a60, 0
	s_waitcnt vmcnt(23)
	v_cvt_f32_f16_e32 v32, v20
	v_cvt_f32_f16_sdwa v33, v20 dst_sel:DWORD dst_unused:UNUSED_PAD src0_sel:WORD_1
	v_cvt_f32_f16_e32 v20, v21
	v_cvt_f32_f16_sdwa v21, v21 dst_sel:DWORD dst_unused:UNUSED_PAD src0_sel:WORD_1
	s_waitcnt vmcnt(22)
	v_cvt_f32_f16_e32 v34, v16
	v_cvt_f32_f16_sdwa v35, v16 dst_sel:DWORD dst_unused:UNUSED_PAD src0_sel:WORD_1
	v_cvt_f32_f16_e32 v16, v17
	v_cvt_f32_f16_sdwa v17, v17 dst_sel:DWORD dst_unused:UNUSED_PAD src0_sel:WORD_1
	s_waitcnt vmcnt(21)
	v_cvt_f32_f16_e32 v46, v24
	v_cvt_f32_f16_sdwa v47, v24 dst_sel:DWORD dst_unused:UNUSED_PAD src0_sel:WORD_1
	v_cvt_f32_f16_e32 v24, v25
	v_cvt_f32_f16_sdwa v25, v25 dst_sel:DWORD dst_unused:UNUSED_PAD src0_sel:WORD_1
	s_waitcnt vmcnt(20)
	v_cvt_f32_f16_e32 v114, v28
	v_cvt_f32_f16_sdwa v115, v28 dst_sel:DWORD dst_unused:UNUSED_PAD src0_sel:WORD_1
	v_cvt_f32_f16_e32 v28, v29
	v_cvt_f32_f16_sdwa v29, v29 dst_sel:DWORD dst_unused:UNUSED_PAD src0_sel:WORD_1
	v_pk_add_f32 v[32:33], v[32:33], 0 op_sel_hi:[1,0]
	v_pk_add_f32 v[20:21], v[20:21], 0 op_sel_hi:[1,0]
	v_pk_add_f32 v[32:33], v[32:33], v[34:35]
	v_pk_add_f32 v[16:17], v[20:21], v[16:17]
	v_pk_add_f32 v[32:33], v[32:33], v[46:47]
	v_pk_add_f32 v[16:17], v[16:17], v[24:25]
	v_pk_add_f32 v[32:33], v[32:33], v[114:115]
	v_pk_add_f32 v[16:17], v[16:17], v[28:29]
	v_cvt_pk_f16_f32 v32, v32, v33
	v_cvt_pk_f16_f32 v33, v16, v17
	v_cvt_f32_f16_e32 v16, v22
	v_cvt_f32_f16_sdwa v17, v22 dst_sel:DWORD dst_unused:UNUSED_PAD src0_sel:WORD_1
	v_cvt_f32_f16_e32 v20, v18
	v_cvt_f32_f16_sdwa v21, v18 dst_sel:DWORD dst_unused:UNUSED_PAD src0_sel:WORD_1
	v_cvt_f32_f16_e32 v24, v26
	v_cvt_f32_f16_sdwa v25, v26 dst_sel:DWORD dst_unused:UNUSED_PAD src0_sel:WORD_1
	v_cvt_f32_f16_e32 v28, v30
	v_cvt_f32_f16_sdwa v29, v30 dst_sel:DWORD dst_unused:UNUSED_PAD src0_sel:WORD_1
	v_pk_add_f32 v[16:17], v[16:17], 0 op_sel_hi:[1,0]
	v_or_b32_e32 v46, 0x800, v44
	v_pk_add_f32 v[16:17], v[16:17], v[20:21]
	v_mov_b32_e32 v47, v39
	v_pk_add_f32 v[16:17], v[16:17], v[24:25]
	v_cvt_f32_f16_e32 v116, v19
	v_pk_add_f32 v[16:17], v[16:17], v[28:29]
	v_lshl_add_u64 v[28:29], v[40:41], 0, v[46:47]
	v_cvt_pk_f16_f32 v34, v16, v17
	v_lshl_add_u64 v[16:17], v[28:29], 0, s[4:5]
	v_cvt_f32_f16_sdwa v117, v19 dst_sel:DWORD dst_unused:UNUSED_PAD src0_sel:WORD_1
	global_load_dwordx4 v[16:19], v[16:17], off
	v_lshl_add_u64 v[20:21], v[28:29], 0, s[8:9]
	v_cvt_f32_f16_e32 v114, v23
	v_cvt_f32_f16_sdwa v115, v23 dst_sel:DWORD dst_unused:UNUSED_PAD src0_sel:WORD_1
	global_load_dwordx4 v[20:23], v[20:21], off
	v_lshl_add_u64 v[24:25], v[28:29], 0, s[12:13]
	v_cvt_f32_f16_e32 v118, v27
	v_cvt_f32_f16_sdwa v119, v27 dst_sel:DWORD dst_unused:UNUSED_PAD src0_sel:WORD_1
	global_load_dwordx4 v[24:27], v[24:25], off
	v_lshl_add_u64 v[28:29], v[28:29], 0, s[2:3]
	v_cvt_f32_f16_e32 v120, v31
	v_cvt_f32_f16_sdwa v121, v31 dst_sel:DWORD dst_unused:UNUSED_PAD src0_sel:WORD_1
	global_load_dwordx4 v[28:31], v[28:29], off
	v_pk_add_f32 v[114:115], v[114:115], 0 op_sel_hi:[1,0]
	v_or_b32_e32 v44, v38, v44
	v_pk_add_f32 v[114:115], v[114:115], v[116:117]
	s_waitcnt vmcnt(14)
	v_cvt_f32_f16_e32 v116, v0
	v_pk_add_f32 v[114:115], v[114:115], v[118:119]
	v_cvt_f32_f16_sdwa v117, v0 dst_sel:DWORD dst_unused:UNUSED_PAD src0_sel:WORD_1
	v_pk_add_f32 v[114:115], v[114:115], v[120:121]
	v_cvt_f32_f16_e32 v0, v1
	v_cvt_pk_f16_f32 v35, v114, v115
	v_cvt_f32_f16_e32 v114, v8
	v_cvt_f32_f16_sdwa v115, v8 dst_sel:DWORD dst_unused:UNUSED_PAD src0_sel:WORD_1
	v_cvt_f32_f16_e32 v8, v9
	v_cvt_f32_f16_sdwa v9, v9 dst_sel:DWORD dst_unused:UNUSED_PAD src0_sel:WORD_1
	v_cvt_f32_f16_sdwa v1, v1 dst_sel:DWORD dst_unused:UNUSED_PAD src0_sel:WORD_1
	s_waitcnt vmcnt(13)
	v_cvt_f32_f16_e32 v118, v4
	v_cvt_f32_f16_sdwa v119, v4 dst_sel:DWORD dst_unused:UNUSED_PAD src0_sel:WORD_1
	ds_write_b128 v44, v[32:35]
	s_waitcnt vmcnt(12)
	v_cvt_f32_f16_e32 v34, v12
	v_cvt_f32_f16_sdwa v35, v12 dst_sel:DWORD dst_unused:UNUSED_PAD src0_sel:WORD_1
	v_pk_add_f32 v[8:9], v[8:9], 0 op_sel_hi:[1,0]
	v_pk_add_f32 v[32:33], v[114:115], 0 op_sel_hi:[1,0]
	v_pk_add_f32 v[0:1], v[8:9], v[0:1]
	v_cvt_f32_f16_e32 v8, v5
	v_cvt_f32_f16_sdwa v9, v5 dst_sel:DWORD dst_unused:UNUSED_PAD src0_sel:WORD_1
	v_pk_add_f32 v[32:33], v[32:33], v[116:117]
	v_cvt_f32_f16_e32 v12, v13
	v_cvt_f32_f16_sdwa v13, v13 dst_sel:DWORD dst_unused:UNUSED_PAD src0_sel:WORD_1
	v_pk_add_f32 v[32:33], v[32:33], v[118:119]
	v_pk_add_f32 v[0:1], v[0:1], v[8:9]
	v_pk_add_f32 v[32:33], v[32:33], v[34:35]
	v_pk_add_f32 v[0:1], v[0:1], v[12:13]
	v_cvt_pk_f16_f32 v4, v32, v33
	v_cvt_f32_f16_e32 v32, v10
	v_cvt_f32_f16_sdwa v33, v10 dst_sel:DWORD dst_unused:UNUSED_PAD src0_sel:WORD_1
	v_cvt_pk_f16_f32 v5, v0, v1
	v_mov_b32_e32 v0, 0xc00
	v_lshl_or_b32 v0, v48, 10, v0
	v_mov_b32_e32 v1, v39
	v_pk_add_f32 v[8:9], v[32:33], 0 op_sel_hi:[1,0]
	v_lshl_add_u64 v[32:33], v[40:41], 0, v[0:1]
	v_lshl_add_u64 v[34:35], v[32:33], 0, s[4:5]
	global_load_dwordx4 v[114:117], v[34:35], off
	v_lshl_add_u64 v[34:35], v[32:33], 0, s[8:9]
	global_load_dwordx4 v[118:121], v[34:35], off
	v_lshl_add_u64 v[34:35], v[32:33], 0, s[12:13]
	global_load_dwordx4 v[122:125], v[34:35], off
	v_lshl_add_u64 v[32:33], v[32:33], 0, s[2:3]
	global_load_dwordx4 v[32:35], v[32:33], off
	v_cvt_f32_f16_e32 v12, v2
	v_cvt_f32_f16_sdwa v13, v2 dst_sel:DWORD dst_unused:UNUSED_PAD src0_sel:WORD_1
	v_cvt_f32_f16_e32 v126, v6
	v_cvt_f32_f16_sdwa v127, v6 dst_sel:DWORD dst_unused:UNUSED_PAD src0_sel:WORD_1
	v_cvt_f32_f16_e32 v128, v14
	v_cvt_f32_f16_sdwa v129, v14 dst_sel:DWORD dst_unused:UNUSED_PAD src0_sel:WORD_1
	v_pk_add_f32 v[8:9], v[8:9], v[12:13]
	v_cvt_f32_f16_e32 v2, v3
	v_pk_add_f32 v[8:9], v[8:9], v[126:127]
	v_cvt_f32_f16_sdwa v3, v3 dst_sel:DWORD dst_unused:UNUSED_PAD src0_sel:WORD_1
	v_pk_add_f32 v[8:9], v[8:9], v[128:129]
	v_cvt_f32_f16_e32 v10, v7
	v_cvt_pk_f16_f32 v6, v8, v9
	v_cvt_f32_f16_e32 v8, v11
	v_cvt_f32_f16_sdwa v9, v11 dst_sel:DWORD dst_unused:UNUSED_PAD src0_sel:WORD_1
	v_cvt_f32_f16_sdwa v11, v7 dst_sel:DWORD dst_unused:UNUSED_PAD src0_sel:WORD_1
	v_cvt_f32_f16_e32 v12, v15
	v_cvt_f32_f16_sdwa v13, v15 dst_sel:DWORD dst_unused:UNUSED_PAD src0_sel:WORD_1
	v_pk_add_f32 v[8:9], v[8:9], 0 op_sel_hi:[1,0]
	v_or_b32_e32 v1, v38, v42
	v_pk_add_f32 v[2:3], v[8:9], v[2:3]
	v_or_b32_e32 v0, v38, v0
	v_pk_add_f32 v[2:3], v[2:3], v[10:11]
	v_accvgpr_write_b32 a59, 0
	v_pk_add_f32 v[2:3], v[2:3], v[12:13]
	v_accvgpr_write_b32 a58, 0
	v_cvt_pk_f16_f32 v7, v2, v3
	s_waitcnt vmcnt(7)
	v_cvt_f32_f16_e32 v2, v16
	v_cvt_f32_f16_sdwa v3, v16 dst_sel:DWORD dst_unused:UNUSED_PAD src0_sel:WORD_1
	ds_write_b128 v1, v[4:7]
	s_waitcnt vmcnt(6)
	v_cvt_f32_f16_e32 v4, v20
	v_cvt_f32_f16_sdwa v5, v20 dst_sel:DWORD dst_unused:UNUSED_PAD src0_sel:WORD_1
	s_waitcnt vmcnt(5)
	v_cvt_f32_f16_e32 v6, v24
	v_cvt_f32_f16_sdwa v7, v24 dst_sel:DWORD dst_unused:UNUSED_PAD src0_sel:WORD_1
	s_waitcnt vmcnt(4)
	v_cvt_f32_f16_e32 v8, v28
	v_cvt_f32_f16_sdwa v9, v28 dst_sel:DWORD dst_unused:UNUSED_PAD src0_sel:WORD_1
	v_pk_add_f32 v[2:3], v[2:3], 0 op_sel_hi:[1,0]
	v_cvt_f32_f16_e32 v10, v29
	v_pk_add_f32 v[2:3], v[2:3], v[4:5]
	v_cvt_f32_f16_e32 v4, v17
	v_cvt_f32_f16_sdwa v5, v17 dst_sel:DWORD dst_unused:UNUSED_PAD src0_sel:WORD_1
	v_pk_add_f32 v[2:3], v[2:3], v[6:7]
	v_cvt_f32_f16_e32 v6, v21
	v_cvt_f32_f16_sdwa v7, v21 dst_sel:DWORD dst_unused:UNUSED_PAD src0_sel:WORD_1
	v_pk_add_f32 v[2:3], v[2:3], v[8:9]
	v_cvt_f32_f16_e32 v8, v25
	v_cvt_f32_f16_sdwa v9, v25 dst_sel:DWORD dst_unused:UNUSED_PAD src0_sel:WORD_1
	v_cvt_f32_f16_sdwa v11, v29 dst_sel:DWORD dst_unused:UNUSED_PAD src0_sel:WORD_1
	v_pk_add_f32 v[4:5], v[4:5], 0 op_sel_hi:[1,0]
	v_cvt_pk_f16_f32 v2, v2, v3
	v_pk_add_f32 v[4:5], v[4:5], v[6:7]
	v_cvt_f32_f16_e32 v6, v22
	v_pk_add_f32 v[4:5], v[4:5], v[8:9]
	v_cvt_f32_f16_sdwa v7, v22 dst_sel:DWORD dst_unused:UNUSED_PAD src0_sel:WORD_1
	v_pk_add_f32 v[4:5], v[4:5], v[10:11]
	v_cvt_f32_f16_e32 v8, v26
	v_cvt_pk_f16_f32 v3, v4, v5
	v_cvt_f32_f16_e32 v4, v18
	v_cvt_f32_f16_sdwa v5, v18 dst_sel:DWORD dst_unused:UNUSED_PAD src0_sel:WORD_1
	v_cvt_f32_f16_sdwa v9, v26 dst_sel:DWORD dst_unused:UNUSED_PAD src0_sel:WORD_1
	v_cvt_f32_f16_e32 v10, v30
	v_cvt_f32_f16_sdwa v11, v30 dst_sel:DWORD dst_unused:UNUSED_PAD src0_sel:WORD_1
	v_pk_add_f32 v[4:5], v[4:5], 0 op_sel_hi:[1,0]
	v_cvt_f32_f16_e32 v12, v31
	v_pk_add_f32 v[4:5], v[4:5], v[6:7]
	v_cvt_f32_f16_e32 v6, v19
	v_cvt_f32_f16_sdwa v7, v19 dst_sel:DWORD dst_unused:UNUSED_PAD src0_sel:WORD_1
	v_pk_add_f32 v[4:5], v[4:5], v[8:9]
	v_cvt_f32_f16_e32 v8, v23
	v_cvt_f32_f16_sdwa v9, v23 dst_sel:DWORD dst_unused:UNUSED_PAD src0_sel:WORD_1
	v_pk_add_f32 v[4:5], v[4:5], v[10:11]
	v_cvt_f32_f16_e32 v10, v27
	v_cvt_f32_f16_sdwa v11, v27 dst_sel:DWORD dst_unused:UNUSED_PAD src0_sel:WORD_1
	v_cvt_f32_f16_sdwa v13, v31 dst_sel:DWORD dst_unused:UNUSED_PAD src0_sel:WORD_1
	v_pk_add_f32 v[6:7], v[6:7], 0 op_sel_hi:[1,0]
	v_cvt_pk_f16_f32 v4, v4, v5
	v_pk_add_f32 v[6:7], v[6:7], v[8:9]
	v_or_b32_e32 v1, v38, v46
	v_pk_add_f32 v[6:7], v[6:7], v[10:11]
	s_waitcnt vmcnt(0)
	v_cvt_f32_f16_e32 v8, v32
	v_pk_add_f32 v[6:7], v[6:7], v[12:13]
	v_cvt_f32_f16_sdwa v9, v32 dst_sel:DWORD dst_unused:UNUSED_PAD src0_sel:WORD_1
	v_cvt_pk_f16_f32 v5, v6, v7
	ds_write_b128 v1, v[2:5]
	v_cvt_f32_f16_e32 v2, v114
	v_cvt_f32_f16_sdwa v3, v114 dst_sel:DWORD dst_unused:UNUSED_PAD src0_sel:WORD_1
	v_cvt_f32_f16_e32 v4, v118
	v_cvt_f32_f16_sdwa v5, v118 dst_sel:DWORD dst_unused:UNUSED_PAD src0_sel:WORD_1
	v_cvt_f32_f16_e32 v6, v122
	v_cvt_f32_f16_sdwa v7, v122 dst_sel:DWORD dst_unused:UNUSED_PAD src0_sel:WORD_1
	v_pk_add_f32 v[2:3], v[2:3], 0 op_sel_hi:[1,0]
	v_cvt_f32_f16_e32 v10, v33
	v_pk_add_f32 v[2:3], v[2:3], v[4:5]
	v_cvt_f32_f16_e32 v4, v115
	v_cvt_f32_f16_sdwa v5, v115 dst_sel:DWORD dst_unused:UNUSED_PAD src0_sel:WORD_1
	v_pk_add_f32 v[2:3], v[2:3], v[6:7]
	v_cvt_f32_f16_e32 v6, v119
	v_cvt_f32_f16_sdwa v7, v119 dst_sel:DWORD dst_unused:UNUSED_PAD src0_sel:WORD_1
	v_pk_add_f32 v[2:3], v[2:3], v[8:9]
	v_cvt_f32_f16_e32 v8, v123
	v_cvt_f32_f16_sdwa v9, v123 dst_sel:DWORD dst_unused:UNUSED_PAD src0_sel:WORD_1
	v_cvt_f32_f16_sdwa v11, v33 dst_sel:DWORD dst_unused:UNUSED_PAD src0_sel:WORD_1
	v_pk_add_f32 v[4:5], v[4:5], 0 op_sel_hi:[1,0]
	v_cvt_pk_f16_f32 v2, v2, v3
	v_pk_add_f32 v[4:5], v[4:5], v[6:7]
	v_cvt_f32_f16_e32 v6, v120
	v_pk_add_f32 v[4:5], v[4:5], v[8:9]
	v_cvt_f32_f16_sdwa v7, v120 dst_sel:DWORD dst_unused:UNUSED_PAD src0_sel:WORD_1
	v_pk_add_f32 v[4:5], v[4:5], v[10:11]
	v_cvt_f32_f16_e32 v8, v124
	v_cvt_pk_f16_f32 v3, v4, v5
	v_cvt_f32_f16_e32 v4, v116
	v_cvt_f32_f16_sdwa v5, v116 dst_sel:DWORD dst_unused:UNUSED_PAD src0_sel:WORD_1
	v_cvt_f32_f16_sdwa v9, v124 dst_sel:DWORD dst_unused:UNUSED_PAD src0_sel:WORD_1
	v_cvt_f32_f16_e32 v10, v34
	v_cvt_f32_f16_sdwa v11, v34 dst_sel:DWORD dst_unused:UNUSED_PAD src0_sel:WORD_1
	v_pk_add_f32 v[4:5], v[4:5], 0 op_sel_hi:[1,0]
	v_cvt_f32_f16_e32 v12, v35
	v_pk_add_f32 v[4:5], v[4:5], v[6:7]
	v_cvt_f32_f16_e32 v6, v117
	v_cvt_f32_f16_sdwa v7, v117 dst_sel:DWORD dst_unused:UNUSED_PAD src0_sel:WORD_1
	v_pk_add_f32 v[4:5], v[4:5], v[8:9]
	v_cvt_f32_f16_e32 v8, v121
	v_cvt_f32_f16_sdwa v9, v121 dst_sel:DWORD dst_unused:UNUSED_PAD src0_sel:WORD_1
	v_pk_add_f32 v[4:5], v[4:5], v[10:11]
	v_cvt_f32_f16_e32 v10, v125
	v_cvt_f32_f16_sdwa v11, v125 dst_sel:DWORD dst_unused:UNUSED_PAD src0_sel:WORD_1
	v_cvt_f32_f16_sdwa v13, v35 dst_sel:DWORD dst_unused:UNUSED_PAD src0_sel:WORD_1
	v_pk_add_f32 v[6:7], v[6:7], 0 op_sel_hi:[1,0]
	v_cvt_pk_f16_f32 v4, v4, v5
	v_pk_add_f32 v[6:7], v[6:7], v[8:9]
	v_mov_b32_e32 v1, v39
	v_pk_add_f32 v[6:7], v[6:7], v[10:11]
	v_accvgpr_write_b32 a57, 0
	v_pk_add_f32 v[6:7], v[6:7], v[12:13]
	v_accvgpr_write_b32 a56, 0
	v_cvt_pk_f16_f32 v5, v6, v7
	ds_write_b128 v0, v[2:5]
	v_lshlrev_b32_e32 v0, 14, v113
	v_lshl_add_u64 v[0:1], s[6:7], 0, v[0:1]
	v_accvgpr_write_b32 a55, 0
	v_accvgpr_write_b32 a54, 0
	v_accvgpr_write_b32 a53, 0
	v_accvgpr_write_b32 a52, 0
	v_accvgpr_write_b32 a51, 0
	v_accvgpr_write_b32 a50, 0
	v_accvgpr_write_b32 a49, 0
	v_accvgpr_write_b32 a48, 0
	v_lshl_add_u64 v[0:1], v[0:1], 0, v[38:39]
	s_mov_b64 s[2:3], 0
	s_waitcnt vmcnt(0)
	ds_write2st64_b32 v152, v150, v151 offset0:64 offset1:68
	s_waitcnt lgkmcnt(0)
	s_barrier

	.amdhsa_kernel _Z6k4_outPKDv8_DF16_S1_PKfS3_S3_Pf
		.amdhsa_group_segment_fixed_size 18432
		.amdhsa_private_segment_fixed_size 0
		.amdhsa_kernarg_size 48
		.amdhsa_user_sgpr_count 2
		.amdhsa_user_sgpr_dispatch_ptr 0
		.amdhsa_user_sgpr_queue_ptr 0
		.amdhsa_user_sgpr_kernarg_segment_ptr 1
		.amdhsa_user_sgpr_dispatch_id 0
		.amdhsa_user_sgpr_kernarg_preload_length 0
		.amdhsa_user_sgpr_kernarg_preload_offset 0
		.amdhsa_user_sgpr_private_segment_size 0
		.amdhsa_uses_dynamic_stack 0
		.amdhsa_enable_private_segment 0
		.amdhsa_system_sgpr_workgroup_id_x 1
		.amdhsa_system_sgpr_workgroup_id_y 0
		.amdhsa_system_sgpr_workgroup_id_z 0
		.amdhsa_system_sgpr_workgroup_info 0
		.amdhsa_system_vgpr_workitem_id 0
		.amdhsa_next_free_vgpr 220
		.amdhsa_next_free_sgpr 21
		.amdhsa_accum_offset 156
		.amdhsa_reserve_vcc 1
		.amdhsa_float_round_mode_32 0
		.amdhsa_float_round_mode_16_64 0
		.amdhsa_float_denorm_mode_32 3
		.amdhsa_float_denorm_mode_16_64 3
		.amdhsa_dx10_clamp 1
		.amdhsa_ieee_mode 1
		.amdhsa_fp16_overflow 0
		.amdhsa_tg_split 0
		.amdhsa_exception_fp_ieee_invalid_op 0
		.amdhsa_exception_fp_denorm_src 0
		.amdhsa_exception_fp_ieee_div_zero 0
		.amdhsa_exception_fp_ieee_overflow 0
		.amdhsa_exception_fp_ieee_underflow 0
		.amdhsa_exception_fp_ieee_inexact 0
		.amdhsa_exception_int_div_zero 0
	.end_amdhsa_kernel

amdhsa.kernels:
  - .agpr_count:     0
    .args:
      - .actual_access:  read_only
        .address_space:  global
        .offset:         0
        .size:           8
        .value_kind:     global_buffer
      - .actual_access:  read_only
        .address_space:  global
        .offset:         8
        .size:           8
        .value_kind:     global_buffer
      - .actual_access:  read_only
        .address_space:  global
        .offset:         16
        .size:           8
        .value_kind:     global_buffer
      - .actual_access:  read_only
        .address_space:  global
        .offset:         24
        .size:           8
        .value_kind:     global_buffer
      - .actual_access:  write_only
        .address_space:  global
        .offset:         32
        .size:           8
        .value_kind:     global_buffer
      - .actual_access:  write_only
        .address_space:  global
        .offset:         40
        .size:           8
        .value_kind:     global_buffer
    .group_segment_fixed_size: 0
    .kernarg_segment_align: 8
    .kernarg_segment_size: 48
    .language:       OpenCL C
    .language_version:
      - 2
      - 0
    .max_flat_workgroup_size: 256
    .name:           _Z7k0_prepPKfS0_S0_S0_PDv8_DF16_S2_
    .private_segment_fixed_size: 0
    .sgpr_count:     17
    .sgpr_spill_count: 0
    .symbol:         _Z7k0_prepPKfS0_S0_S0_PDv8_DF16_S2_.kd
    .uniform_work_group_size: 1
    .uses_dynamic_stack: false
    .vgpr_count:     14
    .vgpr_spill_count: 0
    .wavefront_size: 64
  - .agpr_count:     0
    .args:
      - .actual_access:  read_only
        .address_space:  global
        .offset:         0
        .size:           8
        .value_kind:     global_buffer
      - .actual_access:  read_only
        .address_space:  global
        .offset:         8
        .size:           8
        .value_kind:     global_buffer
      - .actual_access:  read_only
        .address_space:  global
        .offset:         16
        .size:           8
        .value_kind:     global_buffer
      - .actual_access:  read_only
        .address_space:  global
        .offset:         24
        .size:           8
        .value_kind:     global_buffer
      - .actual_access:  read_only
        .address_space:  global
        .offset:         32
        .size:           8
        .value_kind:     global_buffer
      - .actual_access:  write_only
        .address_space:  global
        .offset:         40
        .size:           8
        .value_kind:     global_buffer
      - .actual_access:  write_only
        .address_space:  global
        .offset:         48
        .size:           8
        .value_kind:     global_buffer
      - .actual_access:  write_only
        .address_space:  global
        .offset:         56
        .size:           8
        .value_kind:     global_buffer
    .group_segment_fixed_size: 65536
    .kernarg_segment_align: 8
    .kernarg_segment_size: 64
    .language:       OpenCL C
    .language_version:
      - 2
      - 0
    .max_flat_workgroup_size: 512
    .name:           _Z7k1_projPKfPKDv8_DF16_S0_S0_S0_PS1_S4_S4_
    .private_segment_fixed_size: 0
    .sgpr_count:     50
    .sgpr_spill_count: 0
    .symbol:         _Z7k1_projPKfPKDv8_DF16_S0_S0_S0_PS1_S4_S4_.kd
    .uniform_work_group_size: 1
    .uses_dynamic_stack: false
    .vgpr_count:     192
    .vgpr_spill_count: 0
    .wavefront_size: 64
  - .agpr_count:     0
    .args:
      - .actual_access:  read_only
        .address_space:  global
        .offset:         0
        .size:           8
        .value_kind:     global_buffer
      - .actual_access:  read_only
        .address_space:  global
        .offset:         8
        .size:           8
        .value_kind:     global_buffer
      - .actual_access:  write_only
        .address_space:  global
        .offset:         16
        .size:           8
        .value_kind:     global_buffer
    .group_segment_fixed_size: 4096
    .kernarg_segment_align: 8
    .kernarg_segment_size: 24
    .language:       OpenCL C
    .language_version:
      - 2
      - 0
    .max_flat_workgroup_size: 512
    .name:           _Z9k2_colsumPKDv8_DF16_S1_Pf
    .private_segment_fixed_size: 0
    .sgpr_count:     30
    .sgpr_spill_count: 0
    .symbol:         _Z9k2_colsumPKDv8_DF16_S1_Pf.kd
    .uniform_work_group_size: 1
    .uses_dynamic_stack: false
    .vgpr_count:     176
    .vgpr_spill_count: 0
    .wavefront_size: 64
  - .agpr_count:     0
    .args:
      - .actual_access:  read_only
        .address_space:  global
        .offset:         0
        .size:           8
        .value_kind:     global_buffer
      - .actual_access:  read_only
        .address_space:  global
        .offset:         8
        .size:           8
        .value_kind:     global_buffer
      - .actual_access:  read_only
        .address_space:  global
        .offset:         16
        .size:           8
        .value_kind:     global_buffer
      - .actual_access:  read_only
        .address_space:  global
        .offset:         24
        .size:           8
        .value_kind:     global_buffer
      - .actual_access:  write_only
        .address_space:  global
        .offset:         32
        .size:           8
        .value_kind:     global_buffer
      - .actual_access:  read_only
        .address_space:  global
        .offset:         40
        .size:           8
        .value_kind:     global_buffer
    .group_segment_fixed_size: 123648
    .kernarg_segment_align: 8
    .kernarg_segment_size: 48
    .language:       OpenCL C
    .language_version:
      - 2
      - 0
    .max_flat_workgroup_size: 512
    .name:           _Z7k3_attnPKDv8_DF16_PKDv4_jS4_S4_PS_PKc
    .private_segment_fixed_size: 0
    .sgpr_count:     46
    .sgpr_spill_count: 0
    .symbol:         _Z7k3_attnPKDv8_DF16_PKDv4_jS4_S4_PS_PKc.kd
    .uniform_work_group_size: 1
    .uses_dynamic_stack: false
    .vgpr_count:     224
    .vgpr_spill_count: 0
    .wavefront_size: 64
  - .agpr_count:     64
    .args:
      - .actual_access:  read_only
        .address_space:  global
        .offset:         0
        .size:           8
        .value_kind:     global_buffer
      - .actual_access:  read_only
        .address_space:  global
        .offset:         8
        .size:           8
        .value_kind:     global_buffer
      - .actual_access:  read_only
        .address_space:  global
        .offset:         16
        .size:           8
        .value_kind:     global_buffer
      - .actual_access:  read_only
        .address_space:  global
        .offset:         24
        .size:           8
        .value_kind:     global_buffer
      - .actual_access:  read_only
        .address_space:  global
        .offset:         32
        .size:           8
        .value_kind:     global_buffer
      - .actual_access:  write_only
        .address_space:  global
        .offset:         40
        .size:           8
        .value_kind:     global_buffer
    .group_segment_fixed_size: 18432
    .kernarg_segment_align: 8
    .kernarg_segment_size: 48
    .language:       OpenCL C
    .language_version:
      - 2
      - 0
    .max_flat_workgroup_size: 256
    .name:           _Z6k4_outPKDv8_DF16_S1_PKfS3_S3_Pf
    .private_segment_fixed_size: 0
    .sgpr_count:     27
    .sgpr_spill_count: 0
    .symbol:         _Z6k4_outPKDv8_DF16_S1_PKfS3_S3_Pf.kd
    .uniform_work_group_size: 1
    .uses_dynamic_stack: false
    .vgpr_count:     220
    .vgpr_spill_count: 0
    .wavefront_size: 64
